# v049 + stacked latency trims: route staging/row hoist, ml_out scan reorder, attention row-max permlane swaps, conv31 DPP wave sums, nt weight stores
# speedup vs baseline: 1.0041x; 1.0041x over previous
.LBB0_568:
	s_ashr_i32 s84, s16, 5
	s_and_b32 s64, s3, 0xf80
	s_add_u32 s26, s28, s13
	s_addc_u32 s27, s29, s14
	global_load_dword v157, v81, s[26:27]
	s_andn2_b64 vcc, exec, s[66:67]
	v_mbcnt_hi_u32_b32 v158, -1, v156
	s_barrier
	s_cbranch_vccnz .LBB0_570
	s_ashr_i32 s85, s84, 31
	s_lshl_b64 s[26:27], s[84:85], 14
	v_readlane_b32 s2, v254, 62
	s_add_u32 s2, s2, s26
	v_readlane_b32 s17, v253, 24
	s_addc_u32 s17, s17, s27
	s_lshl_b32 s85, s64, 2
	s_add_u32 s86, s2, s85
	s_addc_u32 s87, s17, 0
	global_load_dwordx2 v[206:207], v154, s[86:87]
	v_readlane_b32 s2, v253, 20
	s_add_u32 s2, s2, s26
	v_readlane_b32 s17, v253, 22
	s_addc_u32 s17, s17, s27
	s_add_u32 s26, s2, s85
	s_addc_u32 s27, s17, 0
	global_load_dwordx2 v[208:209], v154, s[26:27]
.LBB0_570:
	s_ashr_i32 s26, s16, 8
	s_ashr_i32 s27, s26, 31
	s_lshl_b64 s[26:27], s[26:27], 12
	s_or_b64 s[86:87], s[26:27], s[64:65]
	s_lshl_b32 s2, s84, 7
	v_mov_b32_e32 v11, s87
	v_or_b32_e32 v10, s86, v88
	s_and_b32 s17, s2, 0x380
	v_lshlrev_b64 v[2:3], 11, v[10:11]
	v_lshlrev_b64 v[10:11], 13, v[10:11]
	s_lshl_b32 s64, s17, 1
	v_lshl_add_u64 v[10:11], s[74:75], 0, v[10:11]
	v_lshl_add_u64 v[10:11], v[10:11], 0, s[64:65]
	v_lshl_add_u64 v[10:11], v[10:11], 0, v[80:81]
	v_mov_b32_e32 v27, s87
	v_or_b32_e32 v26, s86, v90
	v_lshl_add_u64 v[50:51], v[84:85], 0, s[64:65]
	v_lshl_add_u64 v[52:53], v[86:87], 0, s[64:65]
	v_add_co_u32_e32 v10, vcc, s35, v10
	v_lshlrev_b64 v[18:19], 11, v[26:27]
	v_lshlrev_b64 v[26:27], 13, v[26:27]
	v_lshl_add_u64 v[4:5], v[50:51], 0, v[2:3]
	v_lshl_add_u64 v[6:7], v[52:53], 0, v[2:3]
	v_addc_co_u32_e32 v11, vcc, 0, v11, vcc
	v_lshl_add_u64 v[42:43], s[28:29], 0, v[98:99]
	s_mov_b32 s2, 0x43400000
	v_lshl_add_u64 v[26:27], s[74:75], 0, v[26:27]
	v_mov_b32_e32 v45, s87
	v_or_b32_e32 v44, s86, v92
	global_load_dwordx4 v[2:5], v[4:5], off
	s_nop 0
	global_load_dwordx4 v[6:9], v[6:7], off
	v_add_co_u32_e32 v14, vcc, s2, v42
	v_lshl_add_u64 v[26:27], v[26:27], 0, s[64:65]
	v_lshlrev_b64 v[34:35], 11, v[44:45]
	v_lshlrev_b64 v[44:45], 13, v[44:45]
	v_addc_co_u32_e32 v15, vcc, 0, v43, vcc
	v_lshl_add_u64 v[26:27], v[26:27], 0, v[80:81]
	v_lshl_add_u64 v[44:45], s[74:75], 0, v[44:45]
	global_load_dwordx4 v[10:13], v[10:11], off
	s_nop 0
	global_load_dwordx4 v[14:17], v[14:15], off
	v_lshl_add_u64 v[20:21], v[50:51], 0, v[18:19]
	v_lshl_add_u64 v[22:23], v[52:53], 0, v[18:19]
	v_add_co_u32_e32 v26, vcc, s35, v26
	v_lshl_add_u64 v[44:45], v[44:45], 0, s[64:65]
	global_load_dwordx4 v[18:21], v[20:21], off
	s_nop 0
	global_load_dwordx4 v[22:25], v[22:23], off
	v_addc_co_u32_e32 v27, vcc, 0, v27, vcc
	v_lshl_add_u64 v[44:45], v[44:45], 0, v[80:81]
	v_lshl_add_u64 v[58:59], s[86:87], 0, v[94:95]
	v_lshl_add_u64 v[30:31], s[28:29], 0, v[100:101]
	v_add_co_u32_e32 v44, vcc, s35, v44
	v_lshlrev_b64 v[54:55], 11, v[58:59]
	v_lshlrev_b64 v[58:59], 13, v[58:59]
	global_load_dwordx4 v[26:29], v[26:27], off
	s_nop 0
	global_load_dwordx4 v[30:33], v[30:31], off
	v_lshl_add_u64 v[36:37], v[50:51], 0, v[34:35]
	v_lshl_add_u64 v[38:39], v[52:53], 0, v[34:35]
	v_addc_co_u32_e32 v45, vcc, 0, v45, vcc
	s_mov_b32 s2, 0x43404000
	v_lshl_add_u64 v[58:59], s[74:75], 0, v[58:59]
	global_load_dwordx4 v[34:37], v[36:37], off
	s_nop 0
	global_load_dwordx4 v[38:41], v[38:39], off
	v_add_co_u32_e32 v46, vcc, s2, v42
	v_lshl_add_u64 v[58:59], v[58:59], 0, s[64:65]
	s_nop 0
	v_addc_co_u32_e32 v47, vcc, 0, v43, vcc
	v_lshl_add_u64 v[58:59], v[58:59], 0, v[80:81]
	global_load_dwordx4 v[42:45], v[44:45], off
	s_nop 0
	global_load_dwordx4 v[46:49], v[46:47], off
	v_lshl_add_u64 v[50:51], v[50:51], 0, v[54:55]
	v_lshl_add_u64 v[54:55], v[52:53], 0, v[54:55]
	v_add_co_u32_e32 v58, vcc, s35, v58
	global_load_dwordx4 v[50:53], v[50:51], off
	s_nop 0
	global_load_dwordx4 v[54:57], v[54:55], off
	v_addc_co_u32_e32 v59, vcc, 0, v59, vcc
	global_load_dwordx4 v[58:61], v[58:59], off
	v_lshl_add_u64 v[62:63], s[28:29], 0, v[102:103]
	global_load_dwordx4 v[62:65], v[62:63], off
	s_andn2_b64 vcc, exec, s[66:67]
	s_cbranch_vccnz .Lmlout_noscan
	v_and_b32_e32 v212, 64, v158
	v_add_u32_e32 v213, -1, v158
	v_cmp_lt_i32_e32 vcc, v213, v212
	v_add_u32_e32 v215, -2, v158
	s_waitcnt vmcnt(17)
	v_max_f32_e32 v210, v207, v207
	v_max_f32_e32 v211, v206, v206
	v_cndmask_b32_e32 v213, v213, v158, vcc
	v_max_f32_e32 v210, v211, v210
	v_lshlrev_b32_e32 v213, 2, v213
	ds_bpermute_b32 v214, v213, v210
	v_cmp_lt_i32_e32 vcc, v215, v212
	ds_write_b64 v135, v[206:207]
	s_waitcnt lgkmcnt(1)
	v_max_f32_e32 v214, v214, v214
	v_max_f32_e32 v214, v210, v214
	v_cndmask_b32_e32 v215, v215, v158, vcc
	v_cndmask_b32_e64 v214, v214, v210, s[70:71]
	v_lshlrev_b32_e32 v215, 2, v215
	ds_bpermute_b32 v215, v215, v214
	s_waitcnt lgkmcnt(0)
	v_max_f32_e32 v215, v215, v215
	v_max_f32_e32 v215, v214, v215
	v_cndmask_b32_e64 v214, v215, v214, s[56:57]
	v_add_u32_e32 v215, -4, v158
	v_cmp_lt_i32_e32 vcc, v215, v212
	s_nop 1
	v_cndmask_b32_e32 v215, v215, v158, vcc
	v_lshlrev_b32_e32 v215, 2, v215
	ds_bpermute_b32 v215, v215, v214
	s_waitcnt lgkmcnt(0)
	v_max_f32_e32 v215, v215, v215
	v_max_f32_e32 v215, v214, v215
	v_cndmask_b32_e64 v214, v215, v214, s[58:59]
	v_add_u32_e32 v215, -8, v158
	v_cmp_lt_i32_e32 vcc, v215, v212
	s_nop 1
	v_cndmask_b32_e32 v215, v215, v158, vcc
	v_lshlrev_b32_e32 v215, 2, v215
	ds_bpermute_b32 v215, v215, v214
	s_waitcnt lgkmcnt(0)
	v_max_f32_e32 v215, v215, v215
	v_max_f32_e32 v215, v214, v215
	v_cndmask_b32_e64 v214, v215, v214, s[60:61]
	v_add_u32_e32 v215, -16, v158
	v_cmp_lt_i32_e32 vcc, v215, v212
	s_nop 1
	v_cndmask_b32_e32 v215, v215, v158, vcc
	v_lshlrev_b32_e32 v215, 2, v215
	ds_bpermute_b32 v215, v215, v214
	s_waitcnt lgkmcnt(0)
	v_max_f32_e32 v215, v215, v215
	v_max_f32_e32 v215, v214, v215
	v_cndmask_b32_e64 v214, v215, v214, s[62:63]
	v_subrev_u32_e32 v215, 32, v158
	v_cmp_lt_i32_e32 vcc, v215, v212
	s_nop 1
	v_cndmask_b32_e32 v212, v215, v158, vcc
	v_lshlrev_b32_e32 v212, 2, v212
	ds_bpermute_b32 v212, v212, v214
	v_max_f32_e32 v215, v214, v214
	s_waitcnt lgkmcnt(0)
	v_max_f32_e32 v212, v212, v212
	v_max_f32_e32 v212, v215, v212
	v_cndmask_b32_e64 v212, v212, v214, s[80:81]
	ds_bpermute_b32 v212, v213, v212
	v_max_f32_e32 v213, v157, v157
	s_waitcnt lgkmcnt(0)
	v_max_f32_e32 v212, v212, v212
	v_max_f32_e32 v212, v212, v213
	v_cndmask_b32_e64 v212, v212, v157, s[70:71]
	v_max_f32_e32 v207, v212, v212
	v_max_f32_e32 v206, v207, v211
	v_max_f32_e32 v207, v207, v210
	ds_write_b64 v136, v[206:207]
	s_waitcnt vmcnt(16)
	ds_write_b64 v137, v[208:209]
.Lmlout_noscan:
	v_add_u32_e32 v66, 0, v131
	s_waitcnt vmcnt(15)
	ds_write_b128 v66, v[2:5]
	s_waitcnt vmcnt(14)
	ds_write_b128 v66, v[6:9] offset:32768
	v_add_u32_e32 v2, s12, v131
	s_waitcnt vmcnt(13)
	ds_write_b128 v2, v[10:13]
	v_add_u32_e32 v2, s33, v131
	s_waitcnt vmcnt(12)
	ds_write_b128 v2, v[14:17]
	v_add_u32_e32 v2, 0, v132
	s_waitcnt vmcnt(11)
	ds_write_b128 v2, v[18:21]
	s_waitcnt vmcnt(10)
	ds_write_b128 v2, v[22:25] offset:32768
	v_add_u32_e32 v2, s12, v132
	s_waitcnt vmcnt(9)
	ds_write_b128 v2, v[26:29]
	v_add_u32_e32 v2, s33, v132
	s_waitcnt vmcnt(8)
	ds_write_b128 v2, v[30:33]
	v_add_u32_e32 v2, 0, v133
	s_waitcnt vmcnt(7)
	ds_write_b128 v2, v[34:37]
	s_waitcnt vmcnt(6)
	ds_write_b128 v2, v[38:41] offset:32768
	v_add_u32_e32 v2, s12, v133
	s_waitcnt vmcnt(5)
	ds_write_b128 v2, v[42:45]
	v_add_u32_e32 v2, s33, v133
	s_waitcnt vmcnt(4)
	ds_write_b128 v2, v[46:49]
	v_add_u32_e32 v2, 0, v134
	s_waitcnt vmcnt(3)
	ds_write_b128 v2, v[50:53]
	s_waitcnt vmcnt(2)
	ds_write_b128 v2, v[54:57] offset:32768
	v_add_u32_e32 v2, s12, v134
	s_waitcnt vmcnt(1)
	ds_write_b128 v2, v[58:61]
	v_add_u32_e32 v2, s33, v134
	s_waitcnt vmcnt(0)
	ds_write_b128 v2, v[62:65]
	s_and_saveexec_b64 s[84:85], s[68:69]
	s_cbranch_execz .LBB0_574
	v_mov_b32_e32 v2, 0
	v_mov_b32_e32 v3, 0
	v_mov_b32_e32 v4, 0
	v_mov_b32_e32 v5, 0
	s_and_saveexec_b64 s[88:89], s[82:83]
	s_cbranch_execz .LBB0_573
	v_lshl_add_u64 v[6:7], s[28:29], 0, v[96:97]
	v_add_co_u32_e32 v2, vcc, 0x390000, v6
	s_mov_b64 s[26:27], 0x390000
	s_nop 0
	v_addc_co_u32_e32 v3, vcc, 0, v7, vcc
	global_load_dwordx4 v[2:5], v[2:3], off
	v_lshl_add_u64 v[6:7], v[6:7], 0, s[26:27]
	global_load_dwordx4 v[6:9], v[6:7], off offset:16
	s_waitcnt vmcnt(1)
	v_cvt_pk_bf16_f32 v2, v2, v3
	v_cvt_pk_bf16_f32 v3, v4, v5
	s_waitcnt vmcnt(0)
	v_cvt_pk_bf16_f32 v4, v6, v7
	v_cvt_pk_bf16_f32 v5, v8, v9
